# MLA steady loops: the wait for the next tile's K-fragment LDS reads moved from in front of the per-tile barrier to behind the next iteration's DMA issue
# baseline (speedup 1.0000x reference)
; template <bool FOX>
; __device__ __forceinline__ void attn_unit(const Args& A, int b, int h, int qb, LAS char* shm, LAS float* dg) {
;     ...
;     for (int t = 1; t < t_end; ++t) {
;         if (t == 1 && 4 < nti) ISSUE_K(t0 + 4, 0);
;         if (t + 4 < nti) ISSUE_K(t0 + t + 4, t % NS);
;         if (t + 2 < nti) ISSUE_V(t0 + t + 2, (t + 2) % NS);
;         SFENCE();
;         { if constexpr (!FOX) { if (t0 + t == tw_last + 1) {
; #pragma unroll
;                   for (int r = 0; r < 16; ++r) negm[r] = -INFINITY;
;                   asm volatile("" : "+v"(negm)); } }
;           const lds_cptr vp = vp0 + ((t - 1) % NS) * VSLOT; float sa = 0.f, sb = 0.f;
; #pragma unroll
;           for (int g = 0; g < 2 * NQ; ++g) {
;               if (!FOX && g == 0) c0 = __builtin_amdgcn_mfma_f32_32x32x16_bf16(kf[0], qr[0], negm, 0, 0, 0);
;               else if (!FOX && g == 1) c1 = __builtin_amdgcn_mfma_f32_32x32x16_bf16(kf[1], qr[0], negm, 0, 0, 0);
;               else if (g & 1) c1 = __builtin_amdgcn_mfma_f32_32x32x16_bf16(kf[g], qr[g >> 1], c1, 0, 0, 0); else c0 = __builtin_amdgcn_mfma_f32_32x32x16_bf16(kf[g], qr[g >> 1], c0, 0, 0, 0);
;               if (g < 8) { const int i = (g >> 1) + 4 * (g & 1); vlo[i] = vtr(vp + (i >> 2) * 4096 + (i & 3) * 1024); vhi[i] = vtr(vp + (i >> 2) * 4096 + (i & 3) * 1024 + 512);
;                   if (g < 4) { sa += pp0[4 * g]; sb += pp0[4 * g + 1]; sa += pp0[4 * g + 2]; sb += pp0[4 * g + 3]; } else { sa += pp1[4 * g - 16]; sb += pp1[4 * g - 15]; sa += pp1[4 * g - 14]; sb += pp1[4 * g - 13]; }
;                   asm volatile("" : "+v"(sa), "+v"(sb)); }
;               { constexpr int G0 = FOX ? 0 : 4; if (g >= G0) { const int q = 2 * (g - G0);
; #pragma unroll
;                   for (int k = 0; k < 2; ++k) { const int w = q + k; const unsigned pkd = w < 8 ? cvt_pk_bf16(pp0[2 * w], pp0[2 * w + 1]) : cvt_pk_bf16(pp1[2 * w - 16], pp1[2 * w - 15]); pw[w >> 2][w & 3] = pkd; } } }
;               SFENCE();
;           }
;           lrun += sa + sb; }
;         MASKONLY(t);
;         float rm; ROWMAX(rm);
;         bool resc = false;
;         if (__any(rm > THR)) { const float dl = fmaxf(rm, 0.f); mhat += dl;
; #pragma unroll
;             for (int r = 0; r < 16; ++r) { c0[r] -= dl; c1[r] -= dl; }
;             if constexpr (!FOX) {
; #pragma unroll
;                 for (int r = 0; r < 16; ++r) negm[r] = -mhat;
.Lmla_ss1_v:
	s_add_i32 s27, s42, 0x6000
	s_and_b32 s27, s27, 0x6000
	s_add_i32 m0, s27, s93
	v_lshl_add_u64 v[4:5], v[232:233], 0, s[42:43]
	global_load_lds_dwordx4 v[4:5], off
	s_waitcnt lgkmcnt(0)
	s_add_i32 s27, s42, 0x8000
	v_mfma_f32_32x32x16_bf16 v[114:129], v[206:209], v[138:141], v[82:97]
	s_and_b32 s27, s27, 0x6000
	v_add_u32_e32 v3, s27, v247
	ds_read_b64_tr_b16 v[206:207], v3 offset:49152
	ds_read_b64_tr_b16 v[208:209], v3 offset:49664
	v_add_f32_e32 v4, 0, v67
	v_add_f32_e32 v5, 0, v66
	v_add_f32_e32 v4, v69, v4
	v_add_f32_e32 v5, v68, v5
	v_mfma_f32_32x32x16_bf16 v[98:113], v[194:197], v[138:141], v[82:97]
	ds_read_b64_tr_b16 v[194:195], v3 offset:53248
	ds_read_b64_tr_b16 v[196:197], v3 offset:53760
	v_add_f32_e32 v4, v71, v4
	v_add_f32_e32 v5, v70, v5
	v_add_f32_e32 v4, v73, v4
	v_add_f32_e32 v5, v72, v5
	v_mfma_f32_32x32x16_bf16 v[114:129], v[202:205], v[142:145], v[114:129]
	ds_read_b64_tr_b16 v[202:203], v3 offset:50176
	ds_read_b64_tr_b16 v[204:205], v3 offset:50688
	v_add_f32_e32 v4, v75, v4
	v_add_f32_e32 v5, v74, v5
	v_add_f32_e32 v4, v77, v4
	v_add_f32_e32 v5, v76, v5
	v_mfma_f32_32x32x16_bf16 v[98:113], v[186:189], v[142:145], v[98:113]
	ds_read_b64_tr_b16 v[214:215], v3 offset:54272
	ds_read_b64_tr_b16 v[216:217], v3 offset:54784
	v_add_f32_e32 v4, v79, v4
	v_add_f32_e32 v5, v78, v5
	v_add_f32_e32 v4, v81, v4
	v_add_f32_e32 v5, v80, v5
	v_mfma_f32_32x32x16_bf16 v[114:129], v[198:201], v[146:149], v[114:129]
	ds_read_b64_tr_b16 v[210:211], v3 offset:51200
	ds_read_b64_tr_b16 v[212:213], v3 offset:51712
	v_add_f32_e32 v4, v51, v4
	v_add_f32_e32 v5, v50, v5
	v_add_f32_e32 v4, v53, v4
	v_add_f32_e32 v5, v52, v5
	v_mfma_f32_32x32x16_bf16 v[98:113], v[182:185], v[146:149], v[98:113]
	ds_read_b64_tr_b16 v[12:13], v3 offset:55296
	ds_read_b64_tr_b16 v[14:15], v3 offset:55808
	v_add_f32_e32 v4, v55, v4
	v_add_f32_e32 v5, v54, v5
	v_add_f32_e32 v4, v57, v4
	v_add_f32_e32 v5, v56, v5
	v_mfma_f32_32x32x16_bf16 v[114:129], v[190:193], v[150:153], v[114:129]
	ds_read_b64_tr_b16 v[8:9], v3 offset:52224
	ds_read_b64_tr_b16 v[10:11], v3 offset:52736
	v_add_f32_e32 v4, v59, v4
	v_add_f32_e32 v16, v61, v4
	v_add_f32_e32 v4, v58, v5
	v_add_f32_e32 v17, v60, v4
	v_mfma_f32_32x32x16_bf16 v[98:113], v[170:173], v[150:153], v[98:113]
	ds_read_b64_tr_b16 v[4:5], v3 offset:56320
	ds_read_b64_tr_b16 v[6:7], v3 offset:56832
	v_add_f32_e32 v3, v63, v16
	v_add_f32_e32 v16, v62, v17
	v_add_f32_e32 v3, v65, v3
	v_add_f32_e32 v16, v64, v16
	v_mfma_f32_32x32x16_bf16 v[114:129], v[178:181], v[154:157], v[114:129]
	v_cvt_pk_bf16_f32 v178, v50, v51
	v_cvt_pk_bf16_f32 v179, v52, v53
	v_cvt_pk_bf16_f32 v186, v66, v67
	v_cvt_pk_bf16_f32 v187, v68, v69
	v_mfma_f32_32x32x16_bf16 v[98:113], v[166:169], v[154:157], v[98:113]
	v_cvt_pk_bf16_f32 v180, v54, v55
	v_cvt_pk_bf16_f32 v181, v56, v57
	v_cvt_pk_bf16_f32 v188, v70, v71
	v_cvt_pk_bf16_f32 v189, v72, v73
	v_mfma_f32_32x32x16_bf16 v[114:129], v[174:177], v[158:161], v[114:129]
	v_cvt_pk_bf16_f32 v218, v58, v59
	v_cvt_pk_bf16_f32 v219, v60, v61
	v_cvt_pk_bf16_f32 v182, v74, v75
	v_cvt_pk_bf16_f32 v183, v76, v77
	v_mfma_f32_32x32x16_bf16 v[98:113], v[162:165], v[158:161], v[98:113]
	v_cvt_pk_bf16_f32 v220, v62, v63
	v_cvt_pk_bf16_f32 v221, v64, v65
	v_cvt_pk_bf16_f32 v184, v78, v79
	v_cvt_pk_bf16_f32 v185, v80, v81
	v_add_f32_e32 v3, v3, v16
	v_add_f32_e32 v246, v246, v3
	s_nop 3
	s_waitcnt lgkmcnt(0)
	v_mfma_f32_32x32x16_bf16 v[18:33], v[186:189], v[206:209], v[18:33]
	s_add_i32 s27, s26, 1
	s_and_b32 s64, s27, 3
	s_mulk_i32 s64, 0x3000
	v_exp_f32_e32 v66, v114
	v_exp_f32_e32 v67, v115
	v_exp_f32_e32 v68, v116
	v_exp_f32_e32 v69, v117
	v_add_u32_e32 v3, s64, v248
	v_mfma_f32_32x32x16_bf16 v[34:49], v[186:189], v[194:197], v[34:49]
	v_exp_f32_e32 v70, v118
	v_exp_f32_e32 v71, v119
	v_exp_f32_e32 v72, v120
	v_exp_f32_e32 v73, v121
	ds_read_b128 v[206:209], v3
	ds_read_b128 v[194:197], v3 offset:512
	v_mfma_f32_32x32x16_bf16 v[18:33], v[182:185], v[202:205], v[18:33]
	v_exp_f32_e32 v74, v122
	v_exp_f32_e32 v75, v123
	v_exp_f32_e32 v76, v124
	v_exp_f32_e32 v77, v125
	ds_read_b128 v[202:205], v3 offset:2048
	ds_read_b128 v[186:189], v3 offset:2560
	v_mfma_f32_32x32x16_bf16 v[34:49], v[182:185], v[214:217], v[34:49]
	v_exp_f32_e32 v78, v126
	v_exp_f32_e32 v79, v127
	v_exp_f32_e32 v80, v128
	v_exp_f32_e32 v81, v129
	ds_read_b128 v[198:201], v3 offset:4096
	ds_read_b128 v[182:185], v3 offset:4608
	v_mfma_f32_32x32x16_bf16 v[18:33], v[178:181], v[210:213], v[18:33]
	v_exp_f32_e32 v50, v98
	v_exp_f32_e32 v51, v99
	v_exp_f32_e32 v52, v100
	v_exp_f32_e32 v53, v101
	ds_read_b128 v[190:193], v3 offset:6144
	ds_read_b128 v[170:173], v3 offset:6656
	v_mfma_f32_32x32x16_bf16 v[34:49], v[178:181], v[12:15], v[34:49]
	v_exp_f32_e32 v54, v102
	v_exp_f32_e32 v55, v103
	v_exp_f32_e32 v56, v104
	v_exp_f32_e32 v57, v105
	ds_read_b128 v[178:181], v3 offset:8192
	ds_read_b128 v[166:169], v3 offset:8704
	v_mfma_f32_32x32x16_bf16 v[18:33], v[218:221], v[8:11], v[18:33]
	v_exp_f32_e32 v58, v106
	v_exp_f32_e32 v59, v107
	v_exp_f32_e32 v60, v108
	v_exp_f32_e32 v61, v109
	ds_read_b128 v[174:177], v3 offset:10240
	ds_read_b128 v[162:165], v3 offset:10752
	v_mfma_f32_32x32x16_bf16 v[34:49], v[218:221], v[4:7], v[34:49]
	v_exp_f32_e32 v62, v110
	v_exp_f32_e32 v63, v111
	v_exp_f32_e32 v64, v112
	v_exp_f32_e32 v65, v113
	s_waitcnt vmcnt(4)
	s_barrier
	s_add_u32 s42, s42, 0x2000
	s_addc_u32 s43, s43, 0
	v_lshl_add_u64 v[234:235], v[234:235], 0, s[62:63]
	s_cmp_eq_u32 s27, s96
	s_cbranch_scc1 .Lmla_ss_done
	s_mov_b32 s26, s27
	s_add_i32 s64, s26, 3
	s_cmp_lt_u32 s64, s94
	s_cbranch_scc1 .Lmla_ss1_top
	s_branch .Lmla_ss_back

; template <bool FOX>
; __device__ __forceinline__ void attn_unit(const Args& A, int b, int h, int qb, LAS char* shm, LAS float* dg) {
;     ...
;     for (int t = 1; t < t_end; ++t) {
;         if (t == 1 && 4 < nti) ISSUE_K(t0 + 4, 0);
;         if (t + 4 < nti) ISSUE_K(t0 + t + 4, t % NS);
;         if (t + 2 < nti) ISSUE_V(t0 + t + 2, (t + 2) % NS);
;         SFENCE();
;         { if constexpr (!FOX) { if (t0 + t == tw_last + 1) {
; #pragma unroll
;                   for (int r = 0; r < 16; ++r) negm[r] = -INFINITY;
;                   asm volatile("" : "+v"(negm)); } }
;           const lds_cptr vp = vp0 + ((t - 1) % NS) * VSLOT; float sa = 0.f, sb = 0.f;
; #pragma unroll
;           for (int g = 0; g < 2 * NQ; ++g) {
;               if (!FOX && g == 0) c0 = __builtin_amdgcn_mfma_f32_32x32x16_bf16(kf[0], qr[0], negm, 0, 0, 0);
;               else if (!FOX && g == 1) c1 = __builtin_amdgcn_mfma_f32_32x32x16_bf16(kf[1], qr[0], negm, 0, 0, 0);
;               else if (g & 1) c1 = __builtin_amdgcn_mfma_f32_32x32x16_bf16(kf[g], qr[g >> 1], c1, 0, 0, 0); else c0 = __builtin_amdgcn_mfma_f32_32x32x16_bf16(kf[g], qr[g >> 1], c0, 0, 0, 0);
;               if (g < 8) { const int i = (g >> 1) + 4 * (g & 1); vlo[i] = vtr(vp + (i >> 2) * 4096 + (i & 3) * 1024); vhi[i] = vtr(vp + (i >> 2) * 4096 + (i & 3) * 1024 + 512);
;                   if (g < 4) { sa += pp0[4 * g]; sb += pp0[4 * g + 1]; sa += pp0[4 * g + 2]; sb += pp0[4 * g + 3]; } else { sa += pp1[4 * g - 16]; sb += pp1[4 * g - 15]; sa += pp1[4 * g - 14]; sb += pp1[4 * g - 13]; }
;                   asm volatile("" : "+v"(sa), "+v"(sb)); }
;               { constexpr int G0 = FOX ? 0 : 4; if (g >= G0) { const int q = 2 * (g - G0);
; #pragma unroll
;                   for (int k = 0; k < 2; ++k) { const int w = q + k; const unsigned pkd = w < 8 ? cvt_pk_bf16(pp0[2 * w], pp0[2 * w + 1]) : cvt_pk_bf16(pp1[2 * w - 16], pp1[2 * w - 15]); pw[w >> 2][w & 3] = pkd; } } }
;               SFENCE();
;           }
;           lrun += sa + sb; }
;         MASKONLY(t);
;         float rm; ROWMAX(rm);
;         bool resc = false;
;         if (__any(rm > THR)) { const float dl = fmaxf(rm, 0.f); mhat += dl;
; #pragma unroll
;             for (int r = 0; r < 16; ++r) { c0[r] -= dl; c1[r] -= dl; }
;             if constexpr (!FOX) {
; #pragma unroll
;                 for (int r = 0; r < 16; ++r) negm[r] = -mhat;
.Lmla_ss2_v:
	s_add_i32 s27, s42, 0x6000
	s_and_b32 s27, s27, 0x6000
	s_add_i32 m0, s27, s93
	v_lshl_add_u64 v[4:5], v[232:233], 0, s[42:43]
	global_load_lds_dwordx4 v[4:5], off
	s_waitcnt lgkmcnt(0)
	s_add_i32 s27, s42, 0x8000
	v_mfma_f32_32x32x16_bf16 v[114:129], v[206:209], v[138:141], v[82:97]
	s_and_b32 s27, s27, 0x6000
	v_add_u32_e32 v3, s27, v247
	ds_read_b64_tr_b16 v[206:207], v3 offset:49152
	ds_read_b64_tr_b16 v[208:209], v3 offset:49664
	v_add_f32_e32 v4, 0, v67
	v_add_f32_e32 v5, 0, v66
	v_add_f32_e32 v4, v69, v4
	v_add_f32_e32 v5, v68, v5
	v_mfma_f32_32x32x16_bf16 v[98:113], v[194:197], v[138:141], v[82:97]
	ds_read_b64_tr_b16 v[194:195], v3 offset:53248
	ds_read_b64_tr_b16 v[196:197], v3 offset:53760
	v_add_f32_e32 v4, v71, v4
	v_add_f32_e32 v5, v70, v5
	v_add_f32_e32 v4, v73, v4
	v_add_f32_e32 v5, v72, v5
	v_mfma_f32_32x32x16_bf16 v[114:129], v[202:205], v[142:145], v[114:129]
	ds_read_b64_tr_b16 v[202:203], v3 offset:50176
	ds_read_b64_tr_b16 v[204:205], v3 offset:50688
	v_add_f32_e32 v4, v75, v4
	v_add_f32_e32 v5, v74, v5
	v_add_f32_e32 v4, v77, v4
	v_add_f32_e32 v5, v76, v5
	v_mfma_f32_32x32x16_bf16 v[98:113], v[186:189], v[142:145], v[98:113]
	ds_read_b64_tr_b16 v[214:215], v3 offset:54272
	ds_read_b64_tr_b16 v[216:217], v3 offset:54784
	v_add_f32_e32 v4, v79, v4
	v_add_f32_e32 v5, v78, v5
	v_add_f32_e32 v4, v81, v4
	v_add_f32_e32 v5, v80, v5
	v_mfma_f32_32x32x16_bf16 v[114:129], v[198:201], v[146:149], v[114:129]
	ds_read_b64_tr_b16 v[210:211], v3 offset:51200
	ds_read_b64_tr_b16 v[212:213], v3 offset:51712
	v_add_f32_e32 v4, v51, v4
	v_add_f32_e32 v5, v50, v5
	v_add_f32_e32 v4, v53, v4
	v_add_f32_e32 v5, v52, v5
	v_mfma_f32_32x32x16_bf16 v[98:113], v[182:185], v[146:149], v[98:113]
	ds_read_b64_tr_b16 v[12:13], v3 offset:55296
	ds_read_b64_tr_b16 v[14:15], v3 offset:55808
	v_add_f32_e32 v4, v55, v4
	v_add_f32_e32 v5, v54, v5
	v_add_f32_e32 v4, v57, v4
	v_add_f32_e32 v5, v56, v5
	v_mfma_f32_32x32x16_bf16 v[114:129], v[190:193], v[150:153], v[114:129]
	ds_read_b64_tr_b16 v[8:9], v3 offset:52224
	ds_read_b64_tr_b16 v[10:11], v3 offset:52736
	v_add_f32_e32 v4, v59, v4
	v_add_f32_e32 v16, v61, v4
	v_add_f32_e32 v4, v58, v5
	v_add_f32_e32 v17, v60, v4
	v_mfma_f32_32x32x16_bf16 v[98:113], v[170:173], v[150:153], v[98:113]
	ds_read_b64_tr_b16 v[4:5], v3 offset:56320
	ds_read_b64_tr_b16 v[6:7], v3 offset:56832
	v_add_f32_e32 v3, v63, v16
	v_add_f32_e32 v16, v62, v17
	v_add_f32_e32 v3, v65, v3
	v_add_f32_e32 v16, v64, v16
	v_mfma_f32_32x32x16_bf16 v[114:129], v[178:181], v[154:157], v[114:129]
	v_cvt_pk_bf16_f32 v178, v50, v51
	v_cvt_pk_bf16_f32 v179, v52, v53
	v_cvt_pk_bf16_f32 v186, v66, v67
	v_cvt_pk_bf16_f32 v187, v68, v69
	v_mfma_f32_32x32x16_bf16 v[98:113], v[166:169], v[154:157], v[98:113]
	v_cvt_pk_bf16_f32 v180, v54, v55
	v_cvt_pk_bf16_f32 v181, v56, v57
	v_cvt_pk_bf16_f32 v188, v70, v71
	v_cvt_pk_bf16_f32 v189, v72, v73
	v_mfma_f32_32x32x16_bf16 v[114:129], v[174:177], v[158:161], v[114:129]
	v_cvt_pk_bf16_f32 v218, v58, v59
	v_cvt_pk_bf16_f32 v219, v60, v61
	v_cvt_pk_bf16_f32 v182, v74, v75
	v_cvt_pk_bf16_f32 v183, v76, v77
	v_mfma_f32_32x32x16_bf16 v[98:113], v[162:165], v[158:161], v[98:113]
	v_cvt_pk_bf16_f32 v220, v62, v63
	v_cvt_pk_bf16_f32 v221, v64, v65
	v_cvt_pk_bf16_f32 v184, v78, v79
	v_cvt_pk_bf16_f32 v185, v80, v81
	v_add_f32_e32 v3, v3, v16
	v_add_f32_e32 v246, v246, v3
	s_waitcnt vmcnt(3)
	s_waitcnt lgkmcnt(0)
	s_barrier
	v_mfma_f32_32x32x16_bf16 v[18:33], v[186:189], v[206:209], v[18:33]
	s_add_i32 s27, s26, 1
	s_and_b32 s64, s27, 3
	s_mulk_i32 s64, 0x3000
	v_exp_f32_e32 v66, v114
	v_exp_f32_e32 v67, v115
	v_exp_f32_e32 v68, v116
	v_exp_f32_e32 v69, v117
	v_add_u32_e32 v3, s64, v248
	v_mfma_f32_32x32x16_bf16 v[34:49], v[186:189], v[194:197], v[34:49]
	v_exp_f32_e32 v70, v118
	v_exp_f32_e32 v71, v119
	v_exp_f32_e32 v72, v120
	v_exp_f32_e32 v73, v121
	ds_read_b128 v[206:209], v3
	ds_read_b128 v[194:197], v3 offset:512
	v_mfma_f32_32x32x16_bf16 v[18:33], v[182:185], v[202:205], v[18:33]
	v_exp_f32_e32 v74, v122
	v_exp_f32_e32 v75, v123
	v_exp_f32_e32 v76, v124
	v_exp_f32_e32 v77, v125
	ds_read_b128 v[202:205], v3 offset:2048
	ds_read_b128 v[186:189], v3 offset:2560
	v_mfma_f32_32x32x16_bf16 v[34:49], v[182:185], v[214:217], v[34:49]
	v_exp_f32_e32 v78, v126
	v_exp_f32_e32 v79, v127
	v_exp_f32_e32 v80, v128
	v_exp_f32_e32 v81, v129
	ds_read_b128 v[198:201], v3 offset:4096
	ds_read_b128 v[182:185], v3 offset:4608
	v_mfma_f32_32x32x16_bf16 v[18:33], v[178:181], v[210:213], v[18:33]
	v_exp_f32_e32 v50, v98
	v_exp_f32_e32 v51, v99
	v_exp_f32_e32 v52, v100
	v_exp_f32_e32 v53, v101
	ds_read_b128 v[190:193], v3 offset:6144
	ds_read_b128 v[170:173], v3 offset:6656
	v_mfma_f32_32x32x16_bf16 v[34:49], v[178:181], v[12:15], v[34:49]
	v_exp_f32_e32 v54, v102
	v_exp_f32_e32 v55, v103
	v_exp_f32_e32 v56, v104
	v_exp_f32_e32 v57, v105
	ds_read_b128 v[178:181], v3 offset:8192
	ds_read_b128 v[166:169], v3 offset:8704
	v_mfma_f32_32x32x16_bf16 v[18:33], v[218:221], v[8:11], v[18:33]
	v_exp_f32_e32 v58, v106
	v_exp_f32_e32 v59, v107
	v_exp_f32_e32 v60, v108
	v_exp_f32_e32 v61, v109
	ds_read_b128 v[174:177], v3 offset:10240
	ds_read_b128 v[162:165], v3 offset:10752
	v_mfma_f32_32x32x16_bf16 v[34:49], v[218:221], v[4:7], v[34:49]
	v_exp_f32_e32 v62, v110
	v_exp_f32_e32 v63, v111
	v_exp_f32_e32 v64, v112
	v_exp_f32_e32 v65, v113
	s_add_u32 s42, s42, 0x2000
	s_addc_u32 s43, s43, 0
	v_lshl_add_u64 v[234:235], v[234:235], 0, s[62:63]
	s_cmp_eq_u32 s27, s96
	s_cbranch_scc1 .Lmla_ss_done
	s_mov_b32 s26, s27
	s_add_i32 s64, s26, 3
	s_cmp_lt_u32 s64, s94
	s_cbranch_scc1 .Lmla_ss2_top
	s_branch .Lmla_ss_back
.Lmla_ss_back:
	s_waitcnt lgkmcnt(0)
	s_mov_b64 s[60:61], 0
	s_branch .LBB0_825
.Lmla_ss_done:
	s_waitcnt lgkmcnt(0)
	s_mov_b64 s[46:47], -1
	s_mov_b64 s[52:53], -1
	s_mov_b64 s[60:61], 0
	s_branch .LBB0_867
